# v048 + GEMM unit-top vmcnt(0) removed (P2/P4/P9/P14) and the P6/P16 next-unit gather index loads land in their final registers so nothing waits at the unit top
# speedup vs baseline: 1.0021x; 1.0021x over previous
.LBB0_196:
	s_ashr_i32 s15, s14, 31
	s_lshl_b64 s[16:17], s[14:15], 18
	s_add_u32 s16, s96, s16
	s_addc_u32 s17, s97, s17
	s_and_b64 s[18:19], s[2:3], exec
	s_cselect_b32 s15, s17, s23
	s_cselect_b32 s55, s16, s22
	s_ashr_i32 s13, s12, 31
	s_lshl_b64 s[18:19], s[12:13], 18
	s_add_u32 s18, s6, s18
	s_addc_u32 s19, s7, s19
	s_and_b64 s[26:27], s[2:3], exec
	s_cselect_b32 s13, s19, s25
	s_cselect_b32 s56, s18, s24
	s_add_u32 s22, s22, 0x80
	s_addc_u32 s23, s23, 0
	s_add_u32 s57, s24, 0x100
	v_mov_b32_e32 v2, 0
	s_addc_u32 s63, s25, 0
	s_mov_b32 s64, -2
	v_mov_b32_e32 v3, v2
	v_mov_b32_e32 v4, v2
	v_mov_b32_e32 v5, v2
	v_mov_b32_e32 v6, v2
	v_mov_b32_e32 v7, v2
	v_mov_b32_e32 v8, v2
	v_mov_b32_e32 v9, v2
	v_mov_b32_e32 v14, v2
	v_mov_b32_e32 v15, v2
	v_mov_b32_e32 v16, v2
	v_mov_b32_e32 v17, v2
	v_mov_b32_e32 v22, v2
	v_mov_b32_e32 v23, v2
	v_mov_b32_e32 v24, v2
	v_mov_b32_e32 v25, v2
	v_mov_b32_e32 v34, v2
	v_mov_b32_e32 v35, v2
	v_mov_b32_e32 v36, v2
	v_mov_b32_e32 v37, v2
	v_mov_b32_e32 v38, v2
	v_mov_b32_e32 v39, v2
	v_mov_b32_e32 v40, v2
	v_mov_b32_e32 v41, v2
	v_mov_b32_e32 v50, v2
	v_mov_b32_e32 v51, v2
	v_mov_b32_e32 v52, v2
	v_mov_b32_e32 v53, v2
	v_mov_b32_e32 v54, v2
	v_mov_b32_e32 v55, v2
	v_mov_b32_e32 v56, v2
	v_mov_b32_e32 v57, v2
	v_mov_b32_e32 v66, v2
	v_mov_b32_e32 v67, v2
	v_mov_b32_e32 v68, v2
	v_mov_b32_e32 v69, v2
	v_mov_b32_e32 v70, v2
	v_mov_b32_e32 v71, v2
	v_mov_b32_e32 v72, v2
	v_mov_b32_e32 v73, v2
	v_mov_b32_e32 v82, v2
	v_mov_b32_e32 v83, v2
	v_mov_b32_e32 v84, v2
	v_mov_b32_e32 v85, v2
	v_mov_b32_e32 v86, v2
	v_mov_b32_e32 v87, v2
	v_mov_b32_e32 v88, v2
	v_mov_b32_e32 v89, v2
	v_mov_b32_e32 v98, v2
	v_mov_b32_e32 v99, v2
	v_mov_b32_e32 v100, v2
	v_mov_b32_e32 v101, v2
	v_mov_b32_e32 v102, v2
	v_mov_b32_e32 v103, v2
	v_mov_b32_e32 v104, v2
	v_mov_b32_e32 v105, v2
	v_mov_b32_e32 v114, v2
	v_mov_b32_e32 v115, v2
	v_mov_b32_e32 v116, v2
	v_mov_b32_e32 v117, v2
	v_mov_b32_e32 v118, v2
	v_mov_b32_e32 v119, v2
	v_mov_b32_e32 v120, v2
	v_mov_b32_e32 v121, v2
	v_mov_b32_e32 v74, v2
	v_mov_b32_e32 v75, v2
	v_mov_b32_e32 v76, v2
	v_mov_b32_e32 v77, v2
	v_mov_b32_e32 v78, v2
	v_mov_b32_e32 v79, v2
	v_mov_b32_e32 v80, v2
	v_mov_b32_e32 v81, v2
	v_mov_b32_e32 v90, v2
	v_mov_b32_e32 v91, v2
	v_mov_b32_e32 v92, v2
	v_mov_b32_e32 v93, v2
	v_mov_b32_e32 v94, v2
	v_mov_b32_e32 v95, v2
	v_mov_b32_e32 v96, v2
	v_mov_b32_e32 v97, v2
	v_mov_b32_e32 v106, v2
	v_mov_b32_e32 v107, v2
	v_mov_b32_e32 v108, v2
	v_mov_b32_e32 v109, v2
	v_mov_b32_e32 v110, v2
	v_mov_b32_e32 v111, v2
	v_mov_b32_e32 v112, v2
	v_mov_b32_e32 v113, v2
	v_mov_b32_e32 v122, v2
	v_mov_b32_e32 v123, v2
	v_mov_b32_e32 v124, v2
	v_mov_b32_e32 v125, v2
	v_mov_b32_e32 v126, v2
	v_mov_b32_e32 v127, v2
	v_mov_b32_e32 v128, v2
	v_mov_b32_e32 v129, v2
	v_mov_b32_e32 v62, v2
	v_mov_b32_e32 v63, v2
	v_mov_b32_e32 v64, v2
	v_mov_b32_e32 v65, v2
	v_mov_b32_e32 v58, v2
	v_mov_b32_e32 v59, v2
	v_mov_b32_e32 v60, v2
	v_mov_b32_e32 v61, v2
	v_mov_b32_e32 v46, v2
	v_mov_b32_e32 v47, v2
	v_mov_b32_e32 v48, v2
	v_mov_b32_e32 v49, v2
	v_mov_b32_e32 v42, v2
	v_mov_b32_e32 v43, v2
	v_mov_b32_e32 v44, v2
	v_mov_b32_e32 v45, v2
	v_mov_b32_e32 v30, v2
	v_mov_b32_e32 v31, v2
	v_mov_b32_e32 v32, v2
	v_mov_b32_e32 v33, v2
	v_mov_b32_e32 v26, v2
	v_mov_b32_e32 v27, v2
	v_mov_b32_e32 v28, v2
	v_mov_b32_e32 v29, v2
	v_mov_b32_e32 v18, v2
	v_mov_b32_e32 v19, v2
	v_mov_b32_e32 v20, v2
	v_mov_b32_e32 v21, v2
	v_mov_b32_e32 v10, v2
	v_mov_b32_e32 v11, v2
	v_mov_b32_e32 v12, v2
	v_mov_b32_e32 v13, v2

.LBB0_348:
	s_ashr_i32 s11, s10, 31
	s_lshl_b64 s[12:13], s[10:11], 19
	s_add_u32 s12, s92, s12
	s_addc_u32 s13, s93, s13
	s_and_b64 s[14:15], s[2:3], exec
	s_cselect_b32 s11, s13, s21
	s_cselect_b32 s49, s12, s20
	s_ashr_i32 s9, s8, 31
	s_lshl_b64 s[14:15], s[8:9], 19
	s_add_u32 s14, s40, s14
	s_addc_u32 s15, s41, s15
	s_and_b64 s[22:23], s[2:3], exec
	s_cselect_b32 s9, s15, s19
	s_cselect_b32 s50, s14, s18
	s_add_u32 s20, s20, 0x80
	s_addc_u32 s21, s21, 0
	s_add_u32 s51, s18, 0x100
	v_mov_b32_e32 v66, 0
	s_addc_u32 s52, s19, 0
	s_mov_b32 s53, -2
	v_mov_b32_e32 v67, v66
	v_mov_b32_e32 v68, v66
	v_mov_b32_e32 v69, v66
	v_mov_b32_e32 v70, v66
	v_mov_b32_e32 v71, v66
	v_mov_b32_e32 v72, v66
	v_mov_b32_e32 v73, v66
	v_mov_b32_e32 v74, v66
	v_mov_b32_e32 v75, v66
	v_mov_b32_e32 v76, v66
	v_mov_b32_e32 v77, v66
	v_mov_b32_e32 v78, v66
	v_mov_b32_e32 v79, v66
	v_mov_b32_e32 v80, v66
	v_mov_b32_e32 v81, v66
	v_mov_b32_e32 v82, v66
	v_mov_b32_e32 v83, v66
	v_mov_b32_e32 v84, v66
	v_mov_b32_e32 v85, v66
	v_mov_b32_e32 v86, v66
	v_mov_b32_e32 v87, v66
	v_mov_b32_e32 v88, v66
	v_mov_b32_e32 v89, v66
	v_mov_b32_e32 v90, v66
	v_mov_b32_e32 v91, v66
	v_mov_b32_e32 v92, v66
	v_mov_b32_e32 v93, v66
	v_mov_b32_e32 v94, v66
	v_mov_b32_e32 v95, v66
	v_mov_b32_e32 v96, v66
	v_mov_b32_e32 v97, v66
	v_mov_b32_e32 v34, v66
	v_mov_b32_e32 v35, v66
	v_mov_b32_e32 v36, v66
	v_mov_b32_e32 v37, v66
	v_mov_b32_e32 v38, v66
	v_mov_b32_e32 v39, v66
	v_mov_b32_e32 v40, v66
	v_mov_b32_e32 v41, v66
	v_mov_b32_e32 v42, v66
	v_mov_b32_e32 v43, v66
	v_mov_b32_e32 v44, v66
	v_mov_b32_e32 v45, v66
	v_mov_b32_e32 v46, v66
	v_mov_b32_e32 v47, v66
	v_mov_b32_e32 v48, v66
	v_mov_b32_e32 v49, v66
	v_mov_b32_e32 v50, v66
	v_mov_b32_e32 v51, v66
	v_mov_b32_e32 v52, v66
	v_mov_b32_e32 v53, v66
	v_mov_b32_e32 v54, v66
	v_mov_b32_e32 v55, v66
	v_mov_b32_e32 v56, v66
	v_mov_b32_e32 v57, v66
	v_mov_b32_e32 v58, v66
	v_mov_b32_e32 v59, v66
	v_mov_b32_e32 v60, v66
	v_mov_b32_e32 v61, v66
	v_mov_b32_e32 v62, v66
	v_mov_b32_e32 v63, v66
	v_mov_b32_e32 v64, v66
	v_mov_b32_e32 v65, v66
	v_mov_b32_e32 v98, v66
	v_mov_b32_e32 v99, v66
	v_mov_b32_e32 v100, v66
	v_mov_b32_e32 v101, v66
	v_mov_b32_e32 v102, v66
	v_mov_b32_e32 v103, v66
	v_mov_b32_e32 v104, v66
	v_mov_b32_e32 v105, v66
	v_mov_b32_e32 v106, v66
	v_mov_b32_e32 v107, v66
	v_mov_b32_e32 v108, v66
	v_mov_b32_e32 v109, v66
	v_mov_b32_e32 v110, v66
	v_mov_b32_e32 v111, v66
	v_mov_b32_e32 v112, v66
	v_mov_b32_e32 v113, v66
	v_mov_b32_e32 v114, v66
	v_mov_b32_e32 v115, v66
	v_mov_b32_e32 v116, v66
	v_mov_b32_e32 v117, v66
	v_mov_b32_e32 v118, v66
	v_mov_b32_e32 v119, v66
	v_mov_b32_e32 v120, v66
	v_mov_b32_e32 v121, v66
	v_mov_b32_e32 v130, v66
	v_mov_b32_e32 v131, v66
	v_mov_b32_e32 v132, v66
	v_mov_b32_e32 v133, v66
	v_mov_b32_e32 v134, v66
	v_mov_b32_e32 v135, v66
	v_mov_b32_e32 v136, v66
	v_mov_b32_e32 v137, v66
	v_mov_b32_e32 v26, v66
	v_mov_b32_e32 v27, v66
	v_mov_b32_e32 v28, v66
	v_mov_b32_e32 v29, v66
	v_mov_b32_e32 v30, v66
	v_mov_b32_e32 v31, v66
	v_mov_b32_e32 v32, v66
	v_mov_b32_e32 v33, v66
	v_mov_b32_e32 v18, v66
	v_mov_b32_e32 v19, v66
	v_mov_b32_e32 v20, v66
	v_mov_b32_e32 v21, v66
	v_mov_b32_e32 v22, v66
	v_mov_b32_e32 v23, v66
	v_mov_b32_e32 v24, v66
	v_mov_b32_e32 v25, v66
	v_mov_b32_e32 v10, v66
	v_mov_b32_e32 v11, v66
	v_mov_b32_e32 v12, v66
	v_mov_b32_e32 v13, v66
	v_mov_b32_e32 v14, v66
	v_mov_b32_e32 v15, v66
	v_mov_b32_e32 v16, v66
	v_mov_b32_e32 v17, v66
	v_mov_b32_e32 v2, v66
	v_mov_b32_e32 v3, v66
	v_mov_b32_e32 v4, v66
	v_mov_b32_e32 v5, v66
	v_mov_b32_e32 v6, v66
	v_mov_b32_e32 v7, v66
	v_mov_b32_e32 v8, v66
	v_mov_b32_e32 v9, v66

.LBB0_502:
	v_cndmask_b32_e64 v2, 0, 1, s[22:23]
	s_ashr_i32 s1, s0, 31
	v_mov_b32_e32 v22, 0
	v_cmp_ne_u32_e64 s[2:3], 1, v2
	s_andn2_b64 vcc, exec, s[22:23]
	v_mov_b32_e32 v42, v188
	v_mov_b32_e32 v44, v187
	v_mov_b32_e32 v187, 0
	v_mov_b32_e32 v188, 0
	v_mov_b32_e32 v51, 0
	v_mov_b32_e32 v50, 0
	s_cbranch_vccnz .LBB0_504
	s_lshl_b32 s21, s0, 2
	s_add_i32 s21, s21, 0
	s_add_i32 s24, s21, 0x20480
	v_mov_b32_e32 v2, s24
	ds_read_b32 v2, v2
	s_add_i32 s21, s21, 0x20400
	s_lshl_b64 s[24:25], s[0:1], 18
	s_add_u32 s24, s80, s24
	s_addc_u32 s25, s81, s25
	s_waitcnt lgkmcnt(0)
	v_sub_u32_e32 v2, s55, v2
	v_lshlrev_b32_e32 v4, 8, v2
	v_mov_b32_e32 v2, s21
	ds_read_b32 v2, v2
	v_or_b32_e32 v7, 0x80, v4
	s_waitcnt lgkmcnt(0)
	v_add_u32_e32 v6, -1, v2
	v_or_b32_e32 v2, v4, v1
	v_min_i32_e32 v2, v2, v6
	v_ashrrev_i32_e32 v3, 31, v2
	v_lshl_add_u64 v[2:3], v[2:3], 2, s[24:25]
	global_load_dword v50, v[2:3], off
	v_or_b32_e32 v2, v7, v1
	v_min_i32_e32 v2, v2, v6
	v_ashrrev_i32_e32 v3, 31, v2
	v_lshl_add_u64 v[2:3], v[2:3], 2, s[24:25]
	global_load_dword v188, v[2:3], off
	v_or_b32_e32 v3, v4, v171
	v_min_i32_e32 v4, v3, v6
	v_ashrrev_i32_e32 v5, 31, v4
	v_lshl_add_u64 v[4:5], v[4:5], 2, s[24:25]
	v_or_b32_e32 v3, v7, v171
	global_load_dword v51, v[4:5], off
	v_min_i32_e32 v4, v3, v6
	v_ashrrev_i32_e32 v5, 31, v4
	v_lshl_add_u64 v[4:5], v[4:5], 2, s[24:25]
	global_load_dword v187, v[4:5], off
.LBB0_504:
	s_lshl_b64 s[24:25], s[0:1], 21
	s_add_u32 s1, s61, s24
	s_addc_u32 s29, s62, s25
	s_ashr_i32 s21, s20, 31
	s_lshl_b64 s[24:25], s[20:21], 18
	s_add_u32 s24, s1, s24
	s_addc_u32 s25, s29, s25
	s_and_b64 s[30:31], s[22:23], exec
	s_cselect_b32 s1, s25, s19
	s_cselect_b32 s21, s24, s18
	s_add_u32 s29, s18, 0x100
	v_mov_b32_e32 v43, v167
	v_mov_b32_e32 v45, v167
	s_addc_u32 s57, s19, 0
	s_mov_b32 s63, -2
	s_mov_b64 s[40:41], s[8:9]
	v_mov_b32_e32 v23, v22
	v_mov_b32_e32 v24, v22
	v_mov_b32_e32 v25, v22
	v_mov_b32_e32 v58, v22
	v_mov_b32_e32 v59, v22
	v_mov_b32_e32 v60, v22
	v_mov_b32_e32 v61, v22
	v_mov_b32_e32 v82, v22
	v_mov_b32_e32 v83, v22
	v_mov_b32_e32 v84, v22
	v_mov_b32_e32 v85, v22
	v_mov_b32_e32 v90, v22
	v_mov_b32_e32 v91, v22
	v_mov_b32_e32 v92, v22
	v_mov_b32_e32 v93, v22
	v_mov_b32_e32 v2, v22
	v_mov_b32_e32 v3, v22
	v_mov_b32_e32 v4, v22
	v_mov_b32_e32 v5, v22
	v_mov_b32_e32 v10, v22
	v_mov_b32_e32 v11, v22
	v_mov_b32_e32 v12, v22
	v_mov_b32_e32 v13, v22
	v_mov_b32_e32 v18, v22
	v_mov_b32_e32 v19, v22
	v_mov_b32_e32 v20, v22
	v_mov_b32_e32 v21, v22
	v_mov_b32_e32 v26, v22
	v_mov_b32_e32 v27, v22
	v_mov_b32_e32 v28, v22
	v_mov_b32_e32 v29, v22
	v_mov_b32_e32 v38, v22
	v_mov_b32_e32 v39, v22
	v_mov_b32_e32 v40, v22
	v_mov_b32_e32 v41, v22
	v_mov_b32_e32 v62, v22
	v_mov_b32_e32 v63, v22
	v_mov_b32_e32 v64, v22
	v_mov_b32_e32 v65, v22
	v_mov_b32_e32 v86, v22
	v_mov_b32_e32 v87, v22
	v_mov_b32_e32 v88, v22
	v_mov_b32_e32 v89, v22
	v_mov_b32_e32 v94, v22
	v_mov_b32_e32 v95, v22
	v_mov_b32_e32 v96, v22
	v_mov_b32_e32 v97, v22
	v_mov_b32_e32 v98, v22
	v_mov_b32_e32 v99, v22
	v_mov_b32_e32 v100, v22
	v_mov_b32_e32 v101, v22
	v_mov_b32_e32 v106, v22
	v_mov_b32_e32 v107, v22
	v_mov_b32_e32 v108, v22
	v_mov_b32_e32 v109, v22
	v_mov_b32_e32 v114, v22
	v_mov_b32_e32 v115, v22
	v_mov_b32_e32 v116, v22
	v_mov_b32_e32 v117, v22
	v_mov_b32_e32 v122, v22
	v_mov_b32_e32 v123, v22
	v_mov_b32_e32 v124, v22
	v_mov_b32_e32 v125, v22
	v_mov_b32_e32 v130, v22
	v_mov_b32_e32 v131, v22
	v_mov_b32_e32 v132, v22
	v_mov_b32_e32 v133, v22
	v_mov_b32_e32 v138, v22
	v_mov_b32_e32 v139, v22
	v_mov_b32_e32 v140, v22
	v_mov_b32_e32 v141, v22
	v_mov_b32_e32 v146, v22
	v_mov_b32_e32 v147, v22
	v_mov_b32_e32 v148, v22
	v_mov_b32_e32 v149, v22
	v_mov_b32_e32 v154, v22
	v_mov_b32_e32 v155, v22
	v_mov_b32_e32 v156, v22
	v_mov_b32_e32 v157, v22
	v_mov_b32_e32 v102, v22
	v_mov_b32_e32 v103, v22
	v_mov_b32_e32 v104, v22
	v_mov_b32_e32 v105, v22
	v_mov_b32_e32 v110, v22
	v_mov_b32_e32 v111, v22
	v_mov_b32_e32 v112, v22
	v_mov_b32_e32 v113, v22
	v_mov_b32_e32 v118, v22
	v_mov_b32_e32 v119, v22
	v_mov_b32_e32 v120, v22
	v_mov_b32_e32 v121, v22
	v_mov_b32_e32 v126, v22
	v_mov_b32_e32 v127, v22
	v_mov_b32_e32 v128, v22
	v_mov_b32_e32 v129, v22
	v_mov_b32_e32 v134, v22
	v_mov_b32_e32 v135, v22
	v_mov_b32_e32 v136, v22
	v_mov_b32_e32 v137, v22
	v_mov_b32_e32 v142, v22
	v_mov_b32_e32 v143, v22
	v_mov_b32_e32 v144, v22
	v_mov_b32_e32 v145, v22
	v_mov_b32_e32 v150, v22
	v_mov_b32_e32 v151, v22
	v_mov_b32_e32 v152, v22
	v_mov_b32_e32 v153, v22
	v_mov_b32_e32 v158, v22
	v_mov_b32_e32 v159, v22
	v_mov_b32_e32 v160, v22
	v_mov_b32_e32 v161, v22
	v_mov_b32_e32 v34, v22
	v_mov_b32_e32 v35, v22
	v_mov_b32_e32 v36, v22
	v_mov_b32_e32 v37, v22
	v_mov_b32_e32 v30, v22
	v_mov_b32_e32 v31, v22
	v_mov_b32_e32 v32, v22
	v_mov_b32_e32 v33, v22
	v_mov_b32_e32 v14, v22
	v_mov_b32_e32 v15, v22
	v_mov_b32_e32 v16, v22
	v_mov_b32_e32 v17, v22
	v_mov_b32_e32 v6, v22
	v_mov_b32_e32 v7, v22
	v_mov_b32_e32 v8, v22
	v_mov_b32_e32 v9, v22
	s_branch .LBB0_507

.LBB0_729:
	s_ashr_i32 s13, s12, 31
	s_lshl_b64 s[14:15], s[12:13], 18
	s_add_u32 s14, s96, s14
	s_addc_u32 s15, s97, s15
	s_and_b64 s[16:17], s[2:3], exec
	s_cselect_b32 s13, s15, s23
	s_cselect_b32 s46, s14, s22
	s_ashr_i32 s11, s10, 31
	s_lshl_b64 s[16:17], s[10:11], 18
	s_add_u32 s16, s38, s16
	s_addc_u32 s17, s39, s17
	s_and_b64 s[24:25], s[2:3], exec
	s_cselect_b32 s11, s17, s19
	s_cselect_b32 s47, s16, s18
	s_add_u32 s22, s22, 0x80
	s_addc_u32 s23, s23, 0
	s_add_u32 s48, s18, 0x100
	v_mov_b32_e32 v2, 0
	s_addc_u32 s49, s19, 0
	s_mov_b32 s50, -2
	v_mov_b32_e32 v3, v2
	v_mov_b32_e32 v4, v2
	v_mov_b32_e32 v5, v2
	v_mov_b32_e32 v10, v2
	v_mov_b32_e32 v11, v2
	v_mov_b32_e32 v12, v2
	v_mov_b32_e32 v13, v2
	v_mov_b32_e32 v18, v2
	v_mov_b32_e32 v19, v2
	v_mov_b32_e32 v20, v2
	v_mov_b32_e32 v21, v2
	v_mov_b32_e32 v26, v2
	v_mov_b32_e32 v27, v2
	v_mov_b32_e32 v28, v2
	v_mov_b32_e32 v29, v2
	v_mov_b32_e32 v38, v2
	v_mov_b32_e32 v39, v2
	v_mov_b32_e32 v40, v2
	v_mov_b32_e32 v41, v2
	v_mov_b32_e32 v46, v2
	v_mov_b32_e32 v47, v2
	v_mov_b32_e32 v48, v2
	v_mov_b32_e32 v49, v2
	v_mov_b32_e32 v54, v2
	v_mov_b32_e32 v55, v2
	v_mov_b32_e32 v56, v2
	v_mov_b32_e32 v57, v2
	v_mov_b32_e32 v70, v2
	v_mov_b32_e32 v71, v2
	v_mov_b32_e32 v72, v2
	v_mov_b32_e32 v73, v2
	v_mov_b32_e32 v82, v2
	v_mov_b32_e32 v83, v2
	v_mov_b32_e32 v84, v2
	v_mov_b32_e32 v85, v2
	v_mov_b32_e32 v86, v2
	v_mov_b32_e32 v87, v2
	v_mov_b32_e32 v88, v2
	v_mov_b32_e32 v89, v2
	v_mov_b32_e32 v98, v2
	v_mov_b32_e32 v99, v2
	v_mov_b32_e32 v100, v2
	v_mov_b32_e32 v101, v2
	v_mov_b32_e32 v102, v2
	v_mov_b32_e32 v103, v2
	v_mov_b32_e32 v104, v2
	v_mov_b32_e32 v105, v2
	v_mov_b32_e32 v114, v2
	v_mov_b32_e32 v115, v2
	v_mov_b32_e32 v116, v2
	v_mov_b32_e32 v117, v2
	v_mov_b32_e32 v118, v2
	v_mov_b32_e32 v119, v2
	v_mov_b32_e32 v120, v2
	v_mov_b32_e32 v121, v2
	v_mov_b32_e32 v130, v2
	v_mov_b32_e32 v131, v2
	v_mov_b32_e32 v132, v2
	v_mov_b32_e32 v133, v2
	v_mov_b32_e32 v134, v2
	v_mov_b32_e32 v135, v2
	v_mov_b32_e32 v136, v2
	v_mov_b32_e32 v137, v2
	v_mov_b32_e32 v90, v2
	v_mov_b32_e32 v91, v2
	v_mov_b32_e32 v92, v2
	v_mov_b32_e32 v93, v2
	v_mov_b32_e32 v94, v2
	v_mov_b32_e32 v95, v2
	v_mov_b32_e32 v96, v2
	v_mov_b32_e32 v97, v2
	v_mov_b32_e32 v106, v2
	v_mov_b32_e32 v107, v2
	v_mov_b32_e32 v108, v2
	v_mov_b32_e32 v109, v2
	v_mov_b32_e32 v110, v2
	v_mov_b32_e32 v111, v2
	v_mov_b32_e32 v112, v2
	v_mov_b32_e32 v113, v2
	v_mov_b32_e32 v122, v2
	v_mov_b32_e32 v123, v2
	v_mov_b32_e32 v124, v2
	v_mov_b32_e32 v125, v2
	v_mov_b32_e32 v126, v2
	v_mov_b32_e32 v127, v2
	v_mov_b32_e32 v128, v2
	v_mov_b32_e32 v129, v2
	v_mov_b32_e32 v138, v2
	v_mov_b32_e32 v139, v2
	v_mov_b32_e32 v140, v2
	v_mov_b32_e32 v141, v2
	v_mov_b32_e32 v142, v2
	v_mov_b32_e32 v143, v2
	v_mov_b32_e32 v144, v2
	v_mov_b32_e32 v145, v2
	v_mov_b32_e32 v58, v2
	v_mov_b32_e32 v59, v2
	v_mov_b32_e32 v60, v2
	v_mov_b32_e32 v61, v2
	v_mov_b32_e32 v50, v2
	v_mov_b32_e32 v51, v2
	v_mov_b32_e32 v52, v2
	v_mov_b32_e32 v53, v2
	v_mov_b32_e32 v42, v2
	v_mov_b32_e32 v43, v2
	v_mov_b32_e32 v44, v2
	v_mov_b32_e32 v45, v2
	v_mov_b32_e32 v34, v2
	v_mov_b32_e32 v35, v2
	v_mov_b32_e32 v36, v2
	v_mov_b32_e32 v37, v2
	v_mov_b32_e32 v30, v2
	v_mov_b32_e32 v31, v2
	v_mov_b32_e32 v32, v2
	v_mov_b32_e32 v33, v2
	v_mov_b32_e32 v22, v2
	v_mov_b32_e32 v23, v2
	v_mov_b32_e32 v24, v2
	v_mov_b32_e32 v25, v2
	v_mov_b32_e32 v14, v2
	v_mov_b32_e32 v15, v2
	v_mov_b32_e32 v16, v2
	v_mov_b32_e32 v17, v2
	v_mov_b32_e32 v6, v2
	v_mov_b32_e32 v7, v2
	v_mov_b32_e32 v8, v2
	v_mov_b32_e32 v9, v2

.LBB0_2920:
	s_ashr_i32 s11, s10, 31
	s_lshl_b64 s[12:13], s[10:11], 19
	s_add_u32 s12, s92, s12
	s_addc_u32 s13, s93, s13
	s_and_b64 s[14:15], s[2:3], exec
	s_cselect_b32 s11, s13, s21
	s_cselect_b32 s44, s12, s20
	s_ashr_i32 s9, s8, 31
	s_lshl_b64 s[14:15], s[8:9], 19
	v_readlane_b32 s22, v252, 51
	v_readlane_b32 s23, v252, 52
	s_add_u32 s14, s22, s14
	s_addc_u32 s15, s23, s15
	s_and_b64 s[22:23], s[2:3], exec
	s_cselect_b32 s9, s15, s19
	s_cselect_b32 s45, s14, s18
	s_add_u32 s20, s20, 0x80
	s_addc_u32 s21, s21, 0
	s_add_u32 s46, s18, 0x100
	v_mov_b32_e32 v30, 0
	s_addc_u32 s47, s19, 0
	s_mov_b32 s48, -2
	v_mov_b32_e32 v31, v30
	v_mov_b32_e32 v32, v30
	v_mov_b32_e32 v33, v30
	v_mov_b32_e32 v46, v30
	v_mov_b32_e32 v47, v30
	v_mov_b32_e32 v48, v30
	v_mov_b32_e32 v49, v30
	v_mov_b32_e32 v74, v30
	v_mov_b32_e32 v75, v30
	v_mov_b32_e32 v76, v30
	v_mov_b32_e32 v77, v30
	v_mov_b32_e32 v78, v30
	v_mov_b32_e32 v79, v30
	v_mov_b32_e32 v80, v30
	v_mov_b32_e32 v81, v30
	v_mov_b32_e32 v82, v30
	v_mov_b32_e32 v83, v30
	v_mov_b32_e32 v84, v30
	v_mov_b32_e32 v85, v30
	v_mov_b32_e32 v86, v30
	v_mov_b32_e32 v87, v30
	v_mov_b32_e32 v88, v30
	v_mov_b32_e32 v89, v30
	v_mov_b32_e32 v90, v30
	v_mov_b32_e32 v91, v30
	v_mov_b32_e32 v92, v30
	v_mov_b32_e32 v93, v30
	v_mov_b32_e32 v94, v30
	v_mov_b32_e32 v95, v30
	v_mov_b32_e32 v96, v30
	v_mov_b32_e32 v97, v30
	v_mov_b32_e32 v2, v30
	v_mov_b32_e32 v3, v30
	v_mov_b32_e32 v4, v30
	v_mov_b32_e32 v5, v30
	v_mov_b32_e32 v6, v30
	v_mov_b32_e32 v7, v30
	v_mov_b32_e32 v8, v30
	v_mov_b32_e32 v9, v30
	v_mov_b32_e32 v18, v30
	v_mov_b32_e32 v19, v30
	v_mov_b32_e32 v20, v30
	v_mov_b32_e32 v21, v30
	v_mov_b32_e32 v22, v30
	v_mov_b32_e32 v23, v30
	v_mov_b32_e32 v24, v30
	v_mov_b32_e32 v25, v30
	v_mov_b32_e32 v54, v30
	v_mov_b32_e32 v55, v30
	s_waitcnt lgkmcnt(0)
	v_mov_b32_e32 v56, v30
	v_mov_b32_e32 v57, v30
	v_mov_b32_e32 v62, v30
	v_mov_b32_e32 v63, v30
	v_mov_b32_e32 v64, v30
	v_mov_b32_e32 v65, v30
	v_mov_b32_e32 v66, v30
	v_mov_b32_e32 v67, v30
	v_mov_b32_e32 v68, v30
	v_mov_b32_e32 v69, v30
	v_mov_b32_e32 v70, v30
	v_mov_b32_e32 v71, v30
	v_mov_b32_e32 v72, v30
	v_mov_b32_e32 v73, v30
	v_mov_b32_e32 v98, v30
	v_mov_b32_e32 v99, v30
	v_mov_b32_e32 v100, v30
	v_mov_b32_e32 v101, v30
	v_mov_b32_e32 v102, v30
	v_mov_b32_e32 v103, v30
	v_mov_b32_e32 v104, v30
	v_mov_b32_e32 v105, v30
	v_mov_b32_e32 v106, v30
	v_mov_b32_e32 v107, v30
	v_mov_b32_e32 v108, v30
	v_mov_b32_e32 v109, v30
	v_mov_b32_e32 v110, v30
	v_mov_b32_e32 v111, v30
	v_mov_b32_e32 v112, v30
	v_mov_b32_e32 v113, v30
	v_mov_b32_e32 v114, v30
	v_mov_b32_e32 v115, v30
	v_mov_b32_e32 v116, v30
	v_mov_b32_e32 v117, v30
	v_mov_b32_e32 v118, v30
	v_mov_b32_e32 v119, v30
	v_mov_b32_e32 v120, v30
	v_mov_b32_e32 v121, v30
	v_mov_b32_e32 v122, v30
	v_mov_b32_e32 v123, v30
	v_mov_b32_e32 v124, v30
	v_mov_b32_e32 v125, v30
	v_mov_b32_e32 v126, v30
	v_mov_b32_e32 v127, v30
	v_mov_b32_e32 v128, v30
	v_mov_b32_e32 v129, v30
	v_mov_b32_e32 v50, v30
	v_mov_b32_e32 v51, v30
	v_mov_b32_e32 v52, v30
	v_mov_b32_e32 v53, v30
	v_mov_b32_e32 v58, v30
	v_mov_b32_e32 v59, v30
	v_mov_b32_e32 v60, v30
	v_mov_b32_e32 v61, v30
	v_mov_b32_e32 v38, v30
	v_mov_b32_e32 v39, v30
	v_mov_b32_e32 v40, v30
	v_mov_b32_e32 v41, v30
	v_mov_b32_e32 v42, v30
	v_mov_b32_e32 v43, v30
	v_mov_b32_e32 v44, v30
	v_mov_b32_e32 v45, v30
	v_mov_b32_e32 v26, v30
	v_mov_b32_e32 v27, v30
	v_mov_b32_e32 v28, v30
	v_mov_b32_e32 v29, v30
	v_mov_b32_e32 v34, v30
	v_mov_b32_e32 v35, v30
	v_mov_b32_e32 v36, v30
	v_mov_b32_e32 v37, v30
	v_mov_b32_e32 v14, v30
	v_mov_b32_e32 v15, v30
	v_mov_b32_e32 v16, v30
	v_mov_b32_e32 v17, v30
	v_mov_b32_e32 v10, v30
	v_mov_b32_e32 v11, v30
	v_mov_b32_e32 v12, v30
	v_mov_b32_e32 v13, v30

.LBB0_3074:
	v_cndmask_b32_e64 v2, 0, 1, s[22:23]
	s_mov_b32 s63, s58
	s_ashr_i32 s1, s0, 31
	v_mov_b32_e32 v30, 0
	v_cmp_ne_u32_e64 s[2:3], 1, v2
	s_andn2_b64 vcc, exec, s[22:23]
	v_mov_b32_e32 v74, v177
	v_mov_b32_e32 v76, v176
	v_mov_b32_e32 v176, 0
	v_mov_b32_e32 v177, 0
	v_mov_b32_e32 v87, 0
	v_mov_b32_e32 v86, 0
	s_cbranch_vccnz .LBB0_3076
	s_lshl_b32 s19, s0, 2
	s_add_i32 s19, s19, 0
	s_add_i32 s20, s19, 0x20480
	s_add_i32 s19, s19, 0x20400
	v_mov_b32_e32 v2, s20
	v_mov_b32_e32 v3, s19
	ds_read_b32 v2, v2
	ds_read_b32 v3, v3
	s_lshl_b64 s[20:21], s[0:1], 18
	s_add_u32 s20, s80, s20
	s_addc_u32 s21, s81, s21
	s_waitcnt lgkmcnt(0)
	v_sub_u32_e32 v2, s56, v2
	v_lshlrev_b32_e32 v6, 8, v2
	v_add_u32_e32 v8, -1, v3
	v_or_b32_e32 v9, 0x80, v6
	v_or_b32_e32 v2, v6, v1
	v_min_i32_e32 v2, v2, v8
	v_or_b32_e32 v4, v9, v1
	v_or_b32_e32 v6, v6, v171
	v_or_b32_e32 v9, v9, v171
	v_ashrrev_i32_e32 v3, 31, v2
	v_min_i32_e32 v4, v4, v8
	v_min_i32_e32 v6, v6, v8
	v_min_i32_e32 v8, v9, v8
	v_lshl_add_u64 v[2:3], v[2:3], 2, s[20:21]
	v_ashrrev_i32_e32 v5, 31, v4
	v_ashrrev_i32_e32 v7, 31, v6
	v_ashrrev_i32_e32 v9, 31, v8
	v_lshl_add_u64 v[4:5], v[4:5], 2, s[20:21]
	v_lshl_add_u64 v[6:7], v[6:7], 2, s[20:21]
	v_lshl_add_u64 v[8:9], v[8:9], 2, s[20:21]
	global_load_dword v86, v[2:3], off
	s_nop 0
	global_load_dword v177, v[4:5], off
	global_load_dword v87, v[6:7], off
	global_load_dword v176, v[8:9], off
.LBB0_3076:
	s_lshl_b64 s[20:21], s[0:1], 21
	s_add_u32 s1, s33, s20
	s_addc_u32 s27, s36, s21
	s_ashr_i32 s19, s18, 31
	s_lshl_b64 s[20:21], s[18:19], 18
	s_add_u32 s20, s1, s20
	s_addc_u32 s21, s27, s21
	s_and_b64 s[30:31], s[22:23], exec
	s_cselect_b32 s1, s21, s29
	s_cselect_b32 s19, s20, s28
	s_add_u32 s27, s28, 0x100
	v_mov_b32_e32 v75, v167
	v_mov_b32_e32 v77, v167
	s_addc_u32 s58, s29, 0
	s_mov_b32 s59, -2
	s_mov_b64 s[28:29], s[8:9]
	v_mov_b32_e32 v31, v30
	v_mov_b32_e32 v32, v30
	v_mov_b32_e32 v33, v30
	v_mov_b32_e32 v42, v30
	v_mov_b32_e32 v43, v30
	v_mov_b32_e32 v44, v30
	v_mov_b32_e32 v45, v30
	v_mov_b32_e32 v50, v30
	v_mov_b32_e32 v51, v30
	v_mov_b32_e32 v52, v30
	v_mov_b32_e32 v53, v30
	v_mov_b32_e32 v58, v30
	v_mov_b32_e32 v59, v30
	v_mov_b32_e32 v60, v30
	v_mov_b32_e32 v61, v30
	v_mov_b32_e32 v2, v30
	v_mov_b32_e32 v3, v30
	v_mov_b32_e32 v4, v30
	v_mov_b32_e32 v5, v30
	v_mov_b32_e32 v6, v30
	v_mov_b32_e32 v7, v30
	v_mov_b32_e32 v8, v30
	v_mov_b32_e32 v9, v30
	v_mov_b32_e32 v14, v30
	v_mov_b32_e32 v15, v30
	v_mov_b32_e32 v16, v30
	v_mov_b32_e32 v17, v30
	v_mov_b32_e32 v22, v30
	v_mov_b32_e32 v23, v30
	v_mov_b32_e32 v24, v30
	v_mov_b32_e32 v25, v30
	v_mov_b32_e32 v38, v30
	v_mov_b32_e32 v39, v30
	v_mov_b32_e32 v40, v30
	v_mov_b32_e32 v41, v30
	v_mov_b32_e32 v46, v30
	v_mov_b32_e32 v47, v30
	v_mov_b32_e32 v48, v30
	v_mov_b32_e32 v49, v30
	v_mov_b32_e32 v54, v30
	v_mov_b32_e32 v55, v30
	v_mov_b32_e32 v56, v30
	v_mov_b32_e32 v57, v30
	v_mov_b32_e32 v62, v30
	v_mov_b32_e32 v63, v30
	v_mov_b32_e32 v64, v30
	v_mov_b32_e32 v65, v30
	v_mov_b32_e32 v66, v30
	v_mov_b32_e32 v67, v30
	v_mov_b32_e32 v68, v30
	v_mov_b32_e32 v69, v30
	v_mov_b32_e32 v78, v30
	v_mov_b32_e32 v79, v30
	v_mov_b32_e32 v80, v30
	v_mov_b32_e32 v81, v30
	v_mov_b32_e32 v102, v30
	v_mov_b32_e32 v103, v30
	v_mov_b32_e32 v104, v30
	v_mov_b32_e32 v105, v30
	v_mov_b32_e32 v122, v30
	v_mov_b32_e32 v123, v30
	v_mov_b32_e32 v124, v30
	v_mov_b32_e32 v125, v30
	v_mov_b32_e32 v130, v30
	v_mov_b32_e32 v131, v30
	v_mov_b32_e32 v132, v30
	v_mov_b32_e32 v133, v30
	v_mov_b32_e32 v138, v30
	v_mov_b32_e32 v139, v30
	v_mov_b32_e32 v140, v30
	v_mov_b32_e32 v141, v30
	v_mov_b32_e32 v146, v30
	v_mov_b32_e32 v147, v30
	v_mov_b32_e32 v148, v30
	v_mov_b32_e32 v149, v30
	v_mov_b32_e32 v154, v30
	v_mov_b32_e32 v155, v30
	v_mov_b32_e32 v156, v30
	v_mov_b32_e32 v157, v30
	v_mov_b32_e32 v70, v30
	v_mov_b32_e32 v71, v30
	v_mov_b32_e32 v72, v30
	v_mov_b32_e32 v73, v30
	v_mov_b32_e32 v94, v30
	v_mov_b32_e32 v95, v30
	v_mov_b32_e32 v96, v30
	v_mov_b32_e32 v97, v30
	v_mov_b32_e32 v118, v30
	v_mov_b32_e32 v119, v30
	v_mov_b32_e32 v120, v30
	v_mov_b32_e32 v121, v30
	v_mov_b32_e32 v126, v30
	v_mov_b32_e32 v127, v30
	v_mov_b32_e32 v128, v30
	v_mov_b32_e32 v129, v30
	v_mov_b32_e32 v134, v30
	v_mov_b32_e32 v135, v30
	v_mov_b32_e32 v136, v30
	v_mov_b32_e32 v137, v30
	v_mov_b32_e32 v142, v30
	v_mov_b32_e32 v143, v30
	v_mov_b32_e32 v144, v30
	v_mov_b32_e32 v145, v30
	v_mov_b32_e32 v150, v30
	v_mov_b32_e32 v151, v30
	v_mov_b32_e32 v152, v30
	v_mov_b32_e32 v153, v30
	v_mov_b32_e32 v158, v30
	v_mov_b32_e32 v159, v30
	v_mov_b32_e32 v160, v30
	v_mov_b32_e32 v161, v30
	v_mov_b32_e32 v34, v30
	v_mov_b32_e32 v35, v30
	v_mov_b32_e32 v36, v30
	v_mov_b32_e32 v37, v30
	v_mov_b32_e32 v26, v30
	v_mov_b32_e32 v27, v30
	v_mov_b32_e32 v28, v30
	v_mov_b32_e32 v29, v30
	v_mov_b32_e32 v18, v30
	v_mov_b32_e32 v19, v30
	v_mov_b32_e32 v20, v30
	v_mov_b32_e32 v21, v30
	v_mov_b32_e32 v10, v30
	v_mov_b32_e32 v11, v30
	v_mov_b32_e32 v12, v30
	v_mov_b32_e32 v13, v30
	s_branch .LBB0_3079
